# ph16 scatter epilogue rewritten: all 16 x-row loads issued up front, list loads hoisted before K loop; deferral and zero-mfma removed
# baseline (speedup 1.0000x reference)
.LBB0_1776:
	v_lshl_add_u32 v250, s58, 8, v195
	v_lshlrev_b32_e32 v250, 2, v250
	global_load_dword v235, v250, s[36:37]
	global_load_dword v237, v250, s[36:37] offset:64
	global_load_dword v239, v250, s[36:37] offset:128
	global_load_dword v241, v250, s[36:37] offset:192
	global_load_dword v243, v250, s[36:37] offset:512
	global_load_dword v245, v250, s[36:37] offset:576
	global_load_dword v247, v250, s[36:37] offset:640
	global_load_dword v249, v250, s[36:37] offset:704
	global_load_dword v234, v250, s[40:41]
	global_load_dword v236, v250, s[40:41] offset:64
	global_load_dword v238, v250, s[40:41] offset:128
	global_load_dword v240, v250, s[40:41] offset:192
	global_load_dword v242, v250, s[40:41] offset:512
	global_load_dword v244, v250, s[40:41] offset:576
	global_load_dword v246, v250, s[40:41] offset:640
	global_load_dword v248, v250, s[40:41] offset:704
	s_add_u32 s51, s62, 0x100
	v_mov_b32_e32 v70, 0
	v_mov_b32_e32 v1, 0x3ecc95a3
	s_addc_u32 s59, s63, 0
	s_mov_b32 s64, 0
	v_mov_b32_e32 v71, v70
	v_mov_b32_e32 v72, v70
	v_mov_b32_e32 v73, v70
	v_mov_b32_e32 v66, v70
	v_mov_b32_e32 v67, v70
	v_mov_b32_e32 v68, v70
	v_mov_b32_e32 v69, v70
	v_mov_b32_e32 v86, v70
	v_mov_b32_e32 v87, v70
	v_mov_b32_e32 v88, v70
	v_mov_b32_e32 v89, v70
	v_mov_b32_e32 v82, v70
	v_mov_b32_e32 v83, v70
	v_mov_b32_e32 v84, v70
	v_mov_b32_e32 v85, v70
	v_mov_b32_e32 v46, v70
	v_mov_b32_e32 v47, v70
	v_mov_b32_e32 v48, v70
	v_mov_b32_e32 v49, v70
	v_mov_b32_e32 v42, v70
	v_mov_b32_e32 v43, v70
	v_mov_b32_e32 v44, v70
	v_mov_b32_e32 v45, v70
	v_mov_b32_e32 v62, v70
	v_mov_b32_e32 v63, v70
	v_mov_b32_e32 v64, v70
	v_mov_b32_e32 v65, v70
	v_mov_b32_e32 v58, v70
	v_mov_b32_e32 v59, v70
	v_mov_b32_e32 v60, v70
	v_mov_b32_e32 v61, v70
	v_mov_b32_e32 v78, v70
	v_mov_b32_e32 v79, v70
	v_mov_b32_e32 v80, v70
	v_mov_b32_e32 v81, v70
	v_mov_b32_e32 v74, v70
	v_mov_b32_e32 v75, v70
	v_mov_b32_e32 v76, v70
	v_mov_b32_e32 v77, v70
	v_mov_b32_e32 v94, v70
	v_mov_b32_e32 v95, v70
	v_mov_b32_e32 v96, v70
	v_mov_b32_e32 v97, v70
	v_mov_b32_e32 v90, v70
	v_mov_b32_e32 v91, v70
	v_mov_b32_e32 v92, v70
	v_mov_b32_e32 v93, v70
	v_mov_b32_e32 v102, v70
	v_mov_b32_e32 v103, v70
	v_mov_b32_e32 v104, v70
	v_mov_b32_e32 v105, v70
	v_mov_b32_e32 v98, v70
	v_mov_b32_e32 v99, v70
	v_mov_b32_e32 v100, v70
	v_mov_b32_e32 v101, v70
	v_mov_b32_e32 v118, v70
	v_mov_b32_e32 v119, v70
	v_mov_b32_e32 v120, v70
	v_mov_b32_e32 v121, v70
	v_mov_b32_e32 v114, v70
	v_mov_b32_e32 v115, v70
	v_mov_b32_e32 v116, v70
	v_mov_b32_e32 v117, v70
	v_mov_b32_e32 v134, v70
	v_mov_b32_e32 v135, v70
	v_mov_b32_e32 v136, v70
	v_mov_b32_e32 v137, v70
	v_mov_b32_e32 v130, v70
	v_mov_b32_e32 v131, v70
	v_mov_b32_e32 v132, v70
	v_mov_b32_e32 v133, v70
	v_mov_b32_e32 v150, v70
	v_mov_b32_e32 v151, v70
	v_mov_b32_e32 v152, v70
	v_mov_b32_e32 v153, v70
	v_mov_b32_e32 v146, v70
	v_mov_b32_e32 v147, v70
	v_mov_b32_e32 v148, v70
	v_mov_b32_e32 v149, v70
	v_mov_b32_e32 v110, v70
	v_mov_b32_e32 v111, v70
	v_mov_b32_e32 v112, v70
	v_mov_b32_e32 v113, v70
	v_mov_b32_e32 v106, v70
	v_mov_b32_e32 v107, v70
	v_mov_b32_e32 v108, v70
	v_mov_b32_e32 v109, v70
	v_mov_b32_e32 v126, v70
	v_mov_b32_e32 v127, v70
	v_mov_b32_e32 v128, v70
	v_mov_b32_e32 v129, v70
	v_mov_b32_e32 v122, v70
	v_mov_b32_e32 v123, v70
	v_mov_b32_e32 v124, v70
	v_mov_b32_e32 v125, v70
	v_mov_b32_e32 v142, v70
	v_mov_b32_e32 v143, v70
	v_mov_b32_e32 v144, v70
	v_mov_b32_e32 v145, v70
	v_mov_b32_e32 v138, v70
	v_mov_b32_e32 v139, v70
	v_mov_b32_e32 v140, v70
	v_mov_b32_e32 v141, v70
	v_mov_b32_e32 v158, v70
	v_mov_b32_e32 v159, v70
	v_mov_b32_e32 v160, v70
	v_mov_b32_e32 v161, v70
	v_mov_b32_e32 v154, v70
	v_mov_b32_e32 v155, v70
	v_mov_b32_e32 v156, v70
	v_mov_b32_e32 v157, v70
	v_mov_b32_e32 v50, v70
	v_mov_b32_e32 v51, v70
	v_mov_b32_e32 v52, v70
	v_mov_b32_e32 v53, v70
	v_mov_b32_e32 v54, v70
	v_mov_b32_e32 v55, v70
	v_mov_b32_e32 v56, v70
	v_mov_b32_e32 v57, v70
	v_mov_b32_e32 v34, v70
	v_mov_b32_e32 v35, v70
	v_mov_b32_e32 v36, v70
	v_mov_b32_e32 v37, v70
	v_mov_b32_e32 v38, v70
	v_mov_b32_e32 v39, v70
	v_mov_b32_e32 v40, v70
	v_mov_b32_e32 v41, v70

.LBB0_1780:
	v_lshl_or_b32 v199, s90, 8, v197
	s_nop 15
	s_nop 7
	v_lshlrev_b32_e32 v199, 1, v199
	v_and_b32_e32 v166, 0xffff, v235
	v_lshl_add_u32 v166, v166, 11, v199
	global_load_dwordx4 v[2:5], v166, s[26:27]
	global_load_dwordx4 v[6:9], v166, s[26:27] offset:256
	v_and_b32_e32 v208, 0xffff, v237
	v_lshl_add_u32 v208, v208, 11, v199
	global_load_dwordx4 v[10:13], v208, s[26:27]
	global_load_dwordx4 v[14:17], v208, s[26:27] offset:256
	v_and_b32_e32 v166, 0xffff, v239
	v_lshl_add_u32 v166, v166, 11, v199
	global_load_dwordx4 v[18:21], v166, s[26:27]
	global_load_dwordx4 v[22:25], v166, s[26:27] offset:256
	v_and_b32_e32 v208, 0xffff, v241
	v_lshl_add_u32 v208, v208, 11, v199
	global_load_dwordx4 v[26:29], v208, s[26:27]
	global_load_dwordx4 v[30:33], v208, s[26:27] offset:256
	v_and_b32_e32 v166, 0xffff, v243
	v_lshl_add_u32 v166, v166, 11, v199
	global_load_dwordx4 v[170:173], v166, s[26:27]
	global_load_dwordx4 v[174:177], v166, s[26:27] offset:256
	v_and_b32_e32 v208, 0xffff, v245
	v_lshl_add_u32 v208, v208, 11, v199
	global_load_dwordx4 v[186:189], v208, s[26:27]
	global_load_dwordx4 v[190:193], v208, s[26:27] offset:256
	v_and_b32_e32 v166, 0xffff, v247
	v_lshl_add_u32 v166, v166, 11, v199
	global_load_dwordx4 v[200:203], v166, s[26:27]
	global_load_dwordx4 v[204:207], v166, s[26:27] offset:256
	v_and_b32_e32 v208, 0xffff, v249
	v_lshl_add_u32 v208, v208, 11, v199
	global_load_dwordx4 v[210:213], v208, s[26:27]
	global_load_dwordx4 v[214:217], v208, s[26:27] offset:256
	s_waitcnt vmcnt(15)
	v_lshlrev_b32_e32 v218, 16, v2
	v_and_b32_e32 v219, 0xffff0000, v2
	v_lshlrev_b32_e32 v220, 16, v3
	v_and_b32_e32 v221, 0xffff0000, v3
	v_lshlrev_b32_e32 v222, 16, v4
	v_and_b32_e32 v223, 0xffff0000, v4
	v_lshlrev_b32_e32 v250, 16, v5
	v_and_b32_e32 v251, 0xffff0000, v5
	v_pk_fma_f32 v[154:155], v[154:155], v[234:235], v[218:219] op_sel_hi:[1,0,1]
	v_pk_fma_f32 v[156:157], v[156:157], v[234:235], v[220:221] op_sel_hi:[1,0,1]
	v_pk_fma_f32 v[158:159], v[158:159], v[234:235], v[222:223] op_sel_hi:[1,0,1]
	v_pk_fma_f32 v[160:161], v[160:161], v[234:235], v[250:251] op_sel_hi:[1,0,1]
	v_cvt_pk_bf16_f32 v2, v154, v155
	v_cvt_pk_bf16_f32 v3, v156, v157
	v_cvt_pk_bf16_f32 v4, v158, v159
	v_cvt_pk_bf16_f32 v5, v160, v161
	s_waitcnt vmcnt(14)
	v_lshlrev_b32_e32 v218, 16, v6
	v_and_b32_e32 v219, 0xffff0000, v6
	v_lshlrev_b32_e32 v220, 16, v7
	v_and_b32_e32 v221, 0xffff0000, v7
	v_lshlrev_b32_e32 v222, 16, v8
	v_and_b32_e32 v223, 0xffff0000, v8
	v_lshlrev_b32_e32 v250, 16, v9
	v_and_b32_e32 v251, 0xffff0000, v9
	v_pk_fma_f32 v[146:147], v[146:147], v[234:235], v[218:219] op_sel_hi:[1,0,1]
	v_pk_fma_f32 v[148:149], v[148:149], v[234:235], v[220:221] op_sel_hi:[1,0,1]
	v_pk_fma_f32 v[150:151], v[150:151], v[234:235], v[222:223] op_sel_hi:[1,0,1]
	v_pk_fma_f32 v[152:153], v[152:153], v[234:235], v[250:251] op_sel_hi:[1,0,1]
	v_cvt_pk_bf16_f32 v6, v146, v147
	v_cvt_pk_bf16_f32 v7, v148, v149
	v_cvt_pk_bf16_f32 v8, v150, v151
	v_cvt_pk_bf16_f32 v9, v152, v153
	s_waitcnt vmcnt(13)
	v_lshlrev_b32_e32 v218, 16, v10
	v_and_b32_e32 v219, 0xffff0000, v10
	v_lshlrev_b32_e32 v220, 16, v11
	v_and_b32_e32 v221, 0xffff0000, v11
	v_lshlrev_b32_e32 v222, 16, v12
	v_and_b32_e32 v223, 0xffff0000, v12
	v_lshlrev_b32_e32 v250, 16, v13
	v_and_b32_e32 v251, 0xffff0000, v13
	v_pk_fma_f32 v[138:139], v[138:139], v[236:237], v[218:219] op_sel_hi:[1,0,1]
	v_pk_fma_f32 v[140:141], v[140:141], v[236:237], v[220:221] op_sel_hi:[1,0,1]
	v_pk_fma_f32 v[142:143], v[142:143], v[236:237], v[222:223] op_sel_hi:[1,0,1]
	v_pk_fma_f32 v[144:145], v[144:145], v[236:237], v[250:251] op_sel_hi:[1,0,1]
	v_cvt_pk_bf16_f32 v10, v138, v139
	v_cvt_pk_bf16_f32 v11, v140, v141
	v_cvt_pk_bf16_f32 v12, v142, v143
	v_cvt_pk_bf16_f32 v13, v144, v145
	s_waitcnt vmcnt(12)
	v_lshlrev_b32_e32 v218, 16, v14
	v_and_b32_e32 v219, 0xffff0000, v14
	v_lshlrev_b32_e32 v220, 16, v15
	v_and_b32_e32 v221, 0xffff0000, v15
	v_lshlrev_b32_e32 v222, 16, v16
	v_and_b32_e32 v223, 0xffff0000, v16
	v_lshlrev_b32_e32 v250, 16, v17
	v_and_b32_e32 v251, 0xffff0000, v17
	v_pk_fma_f32 v[130:131], v[130:131], v[236:237], v[218:219] op_sel_hi:[1,0,1]
	v_pk_fma_f32 v[132:133], v[132:133], v[236:237], v[220:221] op_sel_hi:[1,0,1]
	v_pk_fma_f32 v[134:135], v[134:135], v[236:237], v[222:223] op_sel_hi:[1,0,1]
	v_pk_fma_f32 v[136:137], v[136:137], v[236:237], v[250:251] op_sel_hi:[1,0,1]
	v_cvt_pk_bf16_f32 v14, v130, v131
	v_cvt_pk_bf16_f32 v15, v132, v133
	v_cvt_pk_bf16_f32 v16, v134, v135
	v_cvt_pk_bf16_f32 v17, v136, v137
	s_waitcnt vmcnt(11)
	v_lshlrev_b32_e32 v218, 16, v18
	v_and_b32_e32 v219, 0xffff0000, v18
	v_lshlrev_b32_e32 v220, 16, v19
	v_and_b32_e32 v221, 0xffff0000, v19
	v_lshlrev_b32_e32 v222, 16, v20
	v_and_b32_e32 v223, 0xffff0000, v20
	v_lshlrev_b32_e32 v250, 16, v21
	v_and_b32_e32 v251, 0xffff0000, v21
	v_pk_fma_f32 v[122:123], v[122:123], v[238:239], v[218:219] op_sel_hi:[1,0,1]
	v_pk_fma_f32 v[124:125], v[124:125], v[238:239], v[220:221] op_sel_hi:[1,0,1]
	v_pk_fma_f32 v[126:127], v[126:127], v[238:239], v[222:223] op_sel_hi:[1,0,1]
	v_pk_fma_f32 v[128:129], v[128:129], v[238:239], v[250:251] op_sel_hi:[1,0,1]
	v_cvt_pk_bf16_f32 v18, v122, v123
	v_cvt_pk_bf16_f32 v19, v124, v125
	v_cvt_pk_bf16_f32 v20, v126, v127
	v_cvt_pk_bf16_f32 v21, v128, v129
	s_waitcnt vmcnt(10)
	v_lshlrev_b32_e32 v218, 16, v22
	v_and_b32_e32 v219, 0xffff0000, v22
	v_lshlrev_b32_e32 v220, 16, v23
	v_and_b32_e32 v221, 0xffff0000, v23
	v_lshlrev_b32_e32 v222, 16, v24
	v_and_b32_e32 v223, 0xffff0000, v24
	v_lshlrev_b32_e32 v250, 16, v25
	v_and_b32_e32 v251, 0xffff0000, v25
	v_pk_fma_f32 v[114:115], v[114:115], v[238:239], v[218:219] op_sel_hi:[1,0,1]
	v_pk_fma_f32 v[116:117], v[116:117], v[238:239], v[220:221] op_sel_hi:[1,0,1]
	v_pk_fma_f32 v[118:119], v[118:119], v[238:239], v[222:223] op_sel_hi:[1,0,1]
	v_pk_fma_f32 v[120:121], v[120:121], v[238:239], v[250:251] op_sel_hi:[1,0,1]
	v_cvt_pk_bf16_f32 v22, v114, v115
	v_cvt_pk_bf16_f32 v23, v116, v117
	v_cvt_pk_bf16_f32 v24, v118, v119
	v_cvt_pk_bf16_f32 v25, v120, v121
	s_waitcnt vmcnt(9)
	v_lshlrev_b32_e32 v218, 16, v26
	v_and_b32_e32 v219, 0xffff0000, v26
	v_lshlrev_b32_e32 v220, 16, v27
	v_and_b32_e32 v221, 0xffff0000, v27
	v_lshlrev_b32_e32 v222, 16, v28
	v_and_b32_e32 v223, 0xffff0000, v28
	v_lshlrev_b32_e32 v250, 16, v29
	v_and_b32_e32 v251, 0xffff0000, v29
	v_pk_fma_f32 v[106:107], v[106:107], v[240:241], v[218:219] op_sel_hi:[1,0,1]
	v_pk_fma_f32 v[108:109], v[108:109], v[240:241], v[220:221] op_sel_hi:[1,0,1]
	v_pk_fma_f32 v[110:111], v[110:111], v[240:241], v[222:223] op_sel_hi:[1,0,1]
	v_pk_fma_f32 v[112:113], v[112:113], v[240:241], v[250:251] op_sel_hi:[1,0,1]
	v_cvt_pk_bf16_f32 v26, v106, v107
	v_cvt_pk_bf16_f32 v27, v108, v109
	v_cvt_pk_bf16_f32 v28, v110, v111
	v_cvt_pk_bf16_f32 v29, v112, v113
	s_waitcnt vmcnt(8)
	v_lshlrev_b32_e32 v218, 16, v30
	v_and_b32_e32 v219, 0xffff0000, v30
	v_lshlrev_b32_e32 v220, 16, v31
	v_and_b32_e32 v221, 0xffff0000, v31
	v_lshlrev_b32_e32 v222, 16, v32
	v_and_b32_e32 v223, 0xffff0000, v32
	v_lshlrev_b32_e32 v250, 16, v33
	v_and_b32_e32 v251, 0xffff0000, v33
	v_pk_fma_f32 v[98:99], v[98:99], v[240:241], v[218:219] op_sel_hi:[1,0,1]
	v_pk_fma_f32 v[100:101], v[100:101], v[240:241], v[220:221] op_sel_hi:[1,0,1]
	v_pk_fma_f32 v[102:103], v[102:103], v[240:241], v[222:223] op_sel_hi:[1,0,1]
	v_pk_fma_f32 v[104:105], v[104:105], v[240:241], v[250:251] op_sel_hi:[1,0,1]
	v_cvt_pk_bf16_f32 v30, v98, v99
	v_cvt_pk_bf16_f32 v31, v100, v101
	v_cvt_pk_bf16_f32 v32, v102, v103
	v_cvt_pk_bf16_f32 v33, v104, v105
	s_waitcnt vmcnt(7)
	v_lshlrev_b32_e32 v218, 16, v170
	v_and_b32_e32 v219, 0xffff0000, v170
	v_lshlrev_b32_e32 v220, 16, v171
	v_and_b32_e32 v221, 0xffff0000, v171
	v_lshlrev_b32_e32 v222, 16, v172
	v_and_b32_e32 v223, 0xffff0000, v172
	v_lshlrev_b32_e32 v250, 16, v173
	v_and_b32_e32 v251, 0xffff0000, v173
	v_pk_fma_f32 v[90:91], v[90:91], v[242:243], v[218:219] op_sel_hi:[1,0,1]
	v_pk_fma_f32 v[92:93], v[92:93], v[242:243], v[220:221] op_sel_hi:[1,0,1]
	v_pk_fma_f32 v[94:95], v[94:95], v[242:243], v[222:223] op_sel_hi:[1,0,1]
	v_pk_fma_f32 v[96:97], v[96:97], v[242:243], v[250:251] op_sel_hi:[1,0,1]
	v_cvt_pk_bf16_f32 v170, v90, v91
	v_cvt_pk_bf16_f32 v171, v92, v93
	v_cvt_pk_bf16_f32 v172, v94, v95
	v_cvt_pk_bf16_f32 v173, v96, v97
	s_waitcnt vmcnt(6)
	v_lshlrev_b32_e32 v218, 16, v174
	v_and_b32_e32 v219, 0xffff0000, v174
	v_lshlrev_b32_e32 v220, 16, v175
	v_and_b32_e32 v221, 0xffff0000, v175
	v_lshlrev_b32_e32 v222, 16, v176
	v_and_b32_e32 v223, 0xffff0000, v176
	v_lshlrev_b32_e32 v250, 16, v177
	v_and_b32_e32 v251, 0xffff0000, v177
	v_pk_fma_f32 v[82:83], v[82:83], v[242:243], v[218:219] op_sel_hi:[1,0,1]
	v_pk_fma_f32 v[84:85], v[84:85], v[242:243], v[220:221] op_sel_hi:[1,0,1]
	v_pk_fma_f32 v[86:87], v[86:87], v[242:243], v[222:223] op_sel_hi:[1,0,1]
	v_pk_fma_f32 v[88:89], v[88:89], v[242:243], v[250:251] op_sel_hi:[1,0,1]
	v_cvt_pk_bf16_f32 v174, v82, v83
	v_cvt_pk_bf16_f32 v175, v84, v85
	v_cvt_pk_bf16_f32 v176, v86, v87
	v_cvt_pk_bf16_f32 v177, v88, v89
	s_waitcnt vmcnt(5)
	v_lshlrev_b32_e32 v218, 16, v186
	v_and_b32_e32 v219, 0xffff0000, v186
	v_lshlrev_b32_e32 v220, 16, v187
	v_and_b32_e32 v221, 0xffff0000, v187
	v_lshlrev_b32_e32 v222, 16, v188
	v_and_b32_e32 v223, 0xffff0000, v188
	v_lshlrev_b32_e32 v250, 16, v189
	v_and_b32_e32 v251, 0xffff0000, v189
	v_pk_fma_f32 v[74:75], v[74:75], v[244:245], v[218:219] op_sel_hi:[1,0,1]
	v_pk_fma_f32 v[76:77], v[76:77], v[244:245], v[220:221] op_sel_hi:[1,0,1]
	v_pk_fma_f32 v[78:79], v[78:79], v[244:245], v[222:223] op_sel_hi:[1,0,1]
	v_pk_fma_f32 v[80:81], v[80:81], v[244:245], v[250:251] op_sel_hi:[1,0,1]
	v_cvt_pk_bf16_f32 v186, v74, v75
	v_cvt_pk_bf16_f32 v187, v76, v77
	v_cvt_pk_bf16_f32 v188, v78, v79
	v_cvt_pk_bf16_f32 v189, v80, v81
	s_waitcnt vmcnt(4)
	v_lshlrev_b32_e32 v218, 16, v190
	v_and_b32_e32 v219, 0xffff0000, v190
	v_lshlrev_b32_e32 v220, 16, v191
	v_and_b32_e32 v221, 0xffff0000, v191
	v_lshlrev_b32_e32 v222, 16, v192
	v_and_b32_e32 v223, 0xffff0000, v192
	v_lshlrev_b32_e32 v250, 16, v193
	v_and_b32_e32 v251, 0xffff0000, v193
	v_pk_fma_f32 v[66:67], v[66:67], v[244:245], v[218:219] op_sel_hi:[1,0,1]
	v_pk_fma_f32 v[68:69], v[68:69], v[244:245], v[220:221] op_sel_hi:[1,0,1]
	v_pk_fma_f32 v[70:71], v[70:71], v[244:245], v[222:223] op_sel_hi:[1,0,1]
	v_pk_fma_f32 v[72:73], v[72:73], v[244:245], v[250:251] op_sel_hi:[1,0,1]
	v_cvt_pk_bf16_f32 v190, v66, v67
	v_cvt_pk_bf16_f32 v191, v68, v69
	v_cvt_pk_bf16_f32 v192, v70, v71
	v_cvt_pk_bf16_f32 v193, v72, v73
	s_waitcnt vmcnt(3)
	v_lshlrev_b32_e32 v218, 16, v200
	v_and_b32_e32 v219, 0xffff0000, v200
	v_lshlrev_b32_e32 v220, 16, v201
	v_and_b32_e32 v221, 0xffff0000, v201
	v_lshlrev_b32_e32 v222, 16, v202
	v_and_b32_e32 v223, 0xffff0000, v202
	v_lshlrev_b32_e32 v250, 16, v203
	v_and_b32_e32 v251, 0xffff0000, v203
	v_pk_fma_f32 v[58:59], v[58:59], v[246:247], v[218:219] op_sel_hi:[1,0,1]
	v_pk_fma_f32 v[60:61], v[60:61], v[246:247], v[220:221] op_sel_hi:[1,0,1]
	v_pk_fma_f32 v[62:63], v[62:63], v[246:247], v[222:223] op_sel_hi:[1,0,1]
	v_pk_fma_f32 v[64:65], v[64:65], v[246:247], v[250:251] op_sel_hi:[1,0,1]
	v_cvt_pk_bf16_f32 v200, v58, v59
	v_cvt_pk_bf16_f32 v201, v60, v61
	v_cvt_pk_bf16_f32 v202, v62, v63
	v_cvt_pk_bf16_f32 v203, v64, v65
	s_waitcnt vmcnt(2)
	v_lshlrev_b32_e32 v218, 16, v204
	v_and_b32_e32 v219, 0xffff0000, v204
	v_lshlrev_b32_e32 v220, 16, v205
	v_and_b32_e32 v221, 0xffff0000, v205
	v_lshlrev_b32_e32 v222, 16, v206
	v_and_b32_e32 v223, 0xffff0000, v206
	v_lshlrev_b32_e32 v250, 16, v207
	v_and_b32_e32 v251, 0xffff0000, v207
	v_pk_fma_f32 v[50:51], v[50:51], v[246:247], v[218:219] op_sel_hi:[1,0,1]
	v_pk_fma_f32 v[52:53], v[52:53], v[246:247], v[220:221] op_sel_hi:[1,0,1]
	v_pk_fma_f32 v[54:55], v[54:55], v[246:247], v[222:223] op_sel_hi:[1,0,1]
	v_pk_fma_f32 v[56:57], v[56:57], v[246:247], v[250:251] op_sel_hi:[1,0,1]
	v_cvt_pk_bf16_f32 v204, v50, v51
	v_cvt_pk_bf16_f32 v205, v52, v53
	v_cvt_pk_bf16_f32 v206, v54, v55
	v_cvt_pk_bf16_f32 v207, v56, v57
	s_waitcnt vmcnt(1)
	v_lshlrev_b32_e32 v218, 16, v210
	v_and_b32_e32 v219, 0xffff0000, v210
	v_lshlrev_b32_e32 v220, 16, v211
	v_and_b32_e32 v221, 0xffff0000, v211
	v_lshlrev_b32_e32 v222, 16, v212
	v_and_b32_e32 v223, 0xffff0000, v212
	v_lshlrev_b32_e32 v250, 16, v213
	v_and_b32_e32 v251, 0xffff0000, v213
	v_pk_fma_f32 v[42:43], v[42:43], v[248:249], v[218:219] op_sel_hi:[1,0,1]
	v_pk_fma_f32 v[44:45], v[44:45], v[248:249], v[220:221] op_sel_hi:[1,0,1]
	v_pk_fma_f32 v[46:47], v[46:47], v[248:249], v[222:223] op_sel_hi:[1,0,1]
	v_pk_fma_f32 v[48:49], v[48:49], v[248:249], v[250:251] op_sel_hi:[1,0,1]
	v_cvt_pk_bf16_f32 v210, v42, v43
	v_cvt_pk_bf16_f32 v211, v44, v45
	v_cvt_pk_bf16_f32 v212, v46, v47
	v_cvt_pk_bf16_f32 v213, v48, v49
	s_waitcnt vmcnt(0)
	v_lshlrev_b32_e32 v218, 16, v214
	v_and_b32_e32 v219, 0xffff0000, v214
	v_lshlrev_b32_e32 v220, 16, v215
	v_and_b32_e32 v221, 0xffff0000, v215
	v_lshlrev_b32_e32 v222, 16, v216
	v_and_b32_e32 v223, 0xffff0000, v216
	v_lshlrev_b32_e32 v250, 16, v217
	v_and_b32_e32 v251, 0xffff0000, v217
	v_pk_fma_f32 v[34:35], v[34:35], v[248:249], v[218:219] op_sel_hi:[1,0,1]
	v_pk_fma_f32 v[36:37], v[36:37], v[248:249], v[220:221] op_sel_hi:[1,0,1]
	v_pk_fma_f32 v[38:39], v[38:39], v[248:249], v[222:223] op_sel_hi:[1,0,1]
	v_pk_fma_f32 v[40:41], v[40:41], v[248:249], v[250:251] op_sel_hi:[1,0,1]
	v_cvt_pk_bf16_f32 v214, v34, v35
	v_cvt_pk_bf16_f32 v215, v36, v37
	v_cvt_pk_bf16_f32 v216, v38, v39
	v_cvt_pk_bf16_f32 v217, v40, v41
	v_and_b32_e32 v166, 0xffff, v235
	v_cmp_gt_i32_e32 vcc, 0, v235
	v_lshl_add_u32 v166, v166, 11, v199
	s_and_saveexec_b64 s[58:59], vcc
	global_store_dwordx4 v166, v[2:5], s[34:35]
	global_store_dwordx4 v166, v[6:9], s[34:35] offset:256
	s_or_b64 exec, exec, s[58:59]
	v_and_b32_e32 v208, 0xffff, v237
	v_cmp_gt_i32_e32 vcc, 0, v237
	v_lshl_add_u32 v208, v208, 11, v199
	s_and_saveexec_b64 s[58:59], vcc
	global_store_dwordx4 v208, v[10:13], s[34:35]
	global_store_dwordx4 v208, v[14:17], s[34:35] offset:256
	s_or_b64 exec, exec, s[58:59]
	v_and_b32_e32 v166, 0xffff, v239
	v_cmp_gt_i32_e32 vcc, 0, v239
	v_lshl_add_u32 v166, v166, 11, v199
	s_and_saveexec_b64 s[58:59], vcc
	global_store_dwordx4 v166, v[18:21], s[34:35]
	global_store_dwordx4 v166, v[22:25], s[34:35] offset:256
	s_or_b64 exec, exec, s[58:59]
	v_and_b32_e32 v208, 0xffff, v241
	v_cmp_gt_i32_e32 vcc, 0, v241
	v_lshl_add_u32 v208, v208, 11, v199
	s_and_saveexec_b64 s[58:59], vcc
	global_store_dwordx4 v208, v[26:29], s[34:35]
	global_store_dwordx4 v208, v[30:33], s[34:35] offset:256
	s_or_b64 exec, exec, s[58:59]
	v_and_b32_e32 v166, 0xffff, v243
	v_cmp_gt_i32_e32 vcc, 0, v243
	v_lshl_add_u32 v166, v166, 11, v199
	s_and_saveexec_b64 s[58:59], vcc
	global_store_dwordx4 v166, v[170:173], s[34:35]
	global_store_dwordx4 v166, v[174:177], s[34:35] offset:256
	s_or_b64 exec, exec, s[58:59]
	v_and_b32_e32 v208, 0xffff, v245
	v_cmp_gt_i32_e32 vcc, 0, v245
	v_lshl_add_u32 v208, v208, 11, v199
	s_and_saveexec_b64 s[58:59], vcc
	global_store_dwordx4 v208, v[186:189], s[34:35]
	global_store_dwordx4 v208, v[190:193], s[34:35] offset:256
	s_or_b64 exec, exec, s[58:59]
	v_and_b32_e32 v166, 0xffff, v247
	v_cmp_gt_i32_e32 vcc, 0, v247
	v_lshl_add_u32 v166, v166, 11, v199
	s_and_saveexec_b64 s[58:59], vcc
	global_store_dwordx4 v166, v[200:203], s[34:35]
	global_store_dwordx4 v166, v[204:207], s[34:35] offset:256
	s_or_b64 exec, exec, s[58:59]
	v_and_b32_e32 v208, 0xffff, v249
	v_cmp_gt_i32_e32 vcc, 0, v249
	v_lshl_add_u32 v208, v208, 11, v199
	s_and_saveexec_b64 s[58:59], vcc
	global_store_dwordx4 v208, v[210:213], s[34:35]
	global_store_dwordx4 v208, v[214:217], s[34:35] offset:256
	s_or_b64 exec, exec, s[58:59]

.LBB0_1801:
	v_lshl_add_u32 v250, s58, 8, v195
	v_lshlrev_b32_e32 v250, 2, v250
	global_load_dword v235, v250, s[36:37]
	global_load_dword v237, v250, s[36:37] offset:64
	global_load_dword v239, v250, s[36:37] offset:128
	global_load_dword v241, v250, s[36:37] offset:192
	global_load_dword v243, v250, s[36:37] offset:512
	global_load_dword v245, v250, s[36:37] offset:576
	global_load_dword v247, v250, s[36:37] offset:640
	global_load_dword v249, v250, s[36:37] offset:704
	global_load_dword v234, v250, s[40:41]
	global_load_dword v236, v250, s[40:41] offset:64
	global_load_dword v238, v250, s[40:41] offset:128
	global_load_dword v240, v250, s[40:41] offset:192
	global_load_dword v242, v250, s[40:41] offset:512
	global_load_dword v244, v250, s[40:41] offset:576
	global_load_dword v246, v250, s[40:41] offset:640
	global_load_dword v248, v250, s[40:41] offset:704
	s_waitcnt vmcnt(0)
	v_mov_b32_e32 v41, 0
	v_mov_b32_e32 v40, v41
	v_mov_b32_e32 v39, v41
	v_mov_b32_e32 v38, v41
	v_mov_b32_e32 v37, v41
	v_mov_b32_e32 v36, v41
	v_mov_b32_e32 v35, v41
	v_mov_b32_e32 v34, v41
	v_mov_b32_e32 v57, v41
	v_mov_b32_e32 v56, v41
	v_mov_b32_e32 v55, v41
	v_mov_b32_e32 v54, v41
	v_mov_b32_e32 v53, v41
	v_mov_b32_e32 v52, v41
	v_mov_b32_e32 v51, v41
	v_mov_b32_e32 v50, v41
	v_mov_b32_e32 v157, v41
	v_mov_b32_e32 v156, v41
	v_mov_b32_e32 v155, v41
	v_mov_b32_e32 v154, v41
	v_mov_b32_e32 v161, v41
	v_mov_b32_e32 v160, v41
	v_mov_b32_e32 v159, v41
	v_mov_b32_e32 v158, v41
	v_mov_b32_e32 v141, v41
	v_mov_b32_e32 v140, v41
	v_mov_b32_e32 v139, v41
	v_mov_b32_e32 v138, v41
	v_mov_b32_e32 v145, v41
	v_mov_b32_e32 v144, v41
	v_mov_b32_e32 v143, v41
	v_mov_b32_e32 v142, v41
	v_mov_b32_e32 v125, v41
	v_mov_b32_e32 v124, v41
	v_mov_b32_e32 v123, v41
	v_mov_b32_e32 v122, v41
	v_mov_b32_e32 v129, v41
	v_mov_b32_e32 v128, v41
	v_mov_b32_e32 v127, v41
	v_mov_b32_e32 v126, v41
	v_mov_b32_e32 v109, v41
	v_mov_b32_e32 v108, v41
	v_mov_b32_e32 v107, v41
	v_mov_b32_e32 v106, v41
	v_mov_b32_e32 v113, v41
	v_mov_b32_e32 v112, v41
	v_mov_b32_e32 v111, v41
	v_mov_b32_e32 v110, v41
	v_mov_b32_e32 v149, v41
	v_mov_b32_e32 v148, v41
	v_mov_b32_e32 v147, v41
	v_mov_b32_e32 v146, v41
	v_mov_b32_e32 v153, v41
	v_mov_b32_e32 v152, v41
	v_mov_b32_e32 v151, v41
	v_mov_b32_e32 v150, v41
	v_mov_b32_e32 v133, v41
	v_mov_b32_e32 v132, v41
	v_mov_b32_e32 v131, v41
	v_mov_b32_e32 v130, v41
	v_mov_b32_e32 v137, v41
	v_mov_b32_e32 v136, v41
	v_mov_b32_e32 v135, v41
	v_mov_b32_e32 v134, v41
	v_mov_b32_e32 v117, v41
	v_mov_b32_e32 v116, v41
	v_mov_b32_e32 v115, v41
	v_mov_b32_e32 v114, v41
	v_mov_b32_e32 v121, v41
	v_mov_b32_e32 v120, v41
	v_mov_b32_e32 v119, v41
	v_mov_b32_e32 v118, v41
	v_mov_b32_e32 v101, v41
	v_mov_b32_e32 v100, v41
	v_mov_b32_e32 v99, v41
	v_mov_b32_e32 v98, v41
	v_mov_b32_e32 v105, v41
	v_mov_b32_e32 v104, v41
	v_mov_b32_e32 v103, v41
	v_mov_b32_e32 v102, v41
	v_mov_b32_e32 v93, v41
	v_mov_b32_e32 v92, v41
	v_mov_b32_e32 v91, v41
	v_mov_b32_e32 v90, v41
	v_mov_b32_e32 v97, v41
	v_mov_b32_e32 v96, v41
	v_mov_b32_e32 v95, v41
	v_mov_b32_e32 v94, v41
	v_mov_b32_e32 v77, v41
	v_mov_b32_e32 v76, v41
	v_mov_b32_e32 v75, v41
	v_mov_b32_e32 v74, v41
	v_mov_b32_e32 v81, v41
	v_mov_b32_e32 v80, v41
	v_mov_b32_e32 v79, v41
	v_mov_b32_e32 v78, v41
	v_mov_b32_e32 v61, v41
	v_mov_b32_e32 v60, v41
	v_mov_b32_e32 v59, v41
	v_mov_b32_e32 v58, v41
	v_mov_b32_e32 v65, v41
	v_mov_b32_e32 v64, v41
	v_mov_b32_e32 v63, v41
	v_mov_b32_e32 v62, v41
	v_mov_b32_e32 v45, v41
	v_mov_b32_e32 v44, v41
	v_mov_b32_e32 v43, v41
	v_mov_b32_e32 v42, v41
	v_mov_b32_e32 v49, v41
	v_mov_b32_e32 v48, v41
	v_mov_b32_e32 v47, v41
	v_mov_b32_e32 v46, v41
	v_mov_b32_e32 v85, v41
	v_mov_b32_e32 v84, v41
	v_mov_b32_e32 v83, v41
	v_mov_b32_e32 v82, v41
	v_mov_b32_e32 v89, v41
	v_mov_b32_e32 v88, v41
	v_mov_b32_e32 v87, v41
	v_mov_b32_e32 v86, v41
	v_mov_b32_e32 v69, v41
	v_mov_b32_e32 v68, v41
	v_mov_b32_e32 v67, v41
	v_mov_b32_e32 v66, v41
	v_mov_b32_e32 v73, v41
	v_mov_b32_e32 v72, v41
	v_mov_b32_e32 v71, v41
	v_mov_b32_e32 v70, v41
	s_and_b64 vcc, exec, s[44:45]
	s_cbranch_vccnz .LBB0_1779
	s_branch .LBB0_1780
